# speedup vs baseline: 1.0064x; 1.0013x over previous
_Z8out_projPKDF16_S0_PKfPf:
	s_load_dwordx8 s[4:11], s[0:1], 0x0
	s_lshl_b32 s1, s2, 5
	s_lshr_b32 s0, s2, 6
	s_and_b32 s3, s1, 0x7e0
	s_mov_b32 s1, 0
	v_lshrrev_b32_e32 v92, 6, v0
	s_lshl_b64 s[12:13], s[0:1], 14
	v_lshl_or_b32 v2, v92, 11, s12
	v_or_b32_e32 v2, s3, v2
	v_mov_b32_e32 v3, s13
	v_and_b32_e32 v1, 63, v0
	v_lshlrev_b64 v[2:3], 8, v[2:3]
	v_lshlrev_b32_e32 v64, 15, v92
	v_mov_b32_e32 v65, 0
	v_and_b32_e32 v93, 31, v0
	v_bfe_u32 v94, v0, 5, 1
	s_waitcnt lgkmcnt(0)
	v_lshl_add_u64 v[2:3], s[4:5], 0, v[2:3]
	v_lshl_add_u64 v[34:35], s[6:7], 0, v[64:65]
	v_lshlrev_b32_e32 v64, 4, v1
	v_lshl_add_u64 v[66:67], v[34:35], 0, v[64:65]
	v_lshlrev_b32_e32 v64, 8, v93
	v_lshl_or_b32 v64, v94, 4, v64
	v_lshl_add_u64 v[68:69], v[2:3], 0, v[64:65]
	s_lshr_b32 s4, s2, 3
	s_mov_b32 s17, 0
	s_add_i32 s14, s4, 0
	s_and_b32 s14, s14, 7
	s_lshl_b32 s16, s14, 5
	v_lshl_add_u64 v[70:71], v[68:69], 0, s[16:17]
	global_load_dwordx4 v[96:99], v[70:71], off
	s_lshl_b32 s16, s14, 12
	v_lshl_add_u64 v[72:73], v[66:67], 0, s[16:17]
	global_load_dwordx4 v[128:131], v[72:73], off
	global_load_dwordx4 v[132:135], v[72:73], off offset:1024
	global_load_dwordx4 v[136:139], v[72:73], off offset:2048
	global_load_dwordx4 v[140:143], v[72:73], off offset:3072
	s_add_i32 s14, s4, 1
	s_and_b32 s14, s14, 7
	s_lshl_b32 s16, s14, 5
	v_lshl_add_u64 v[70:71], v[68:69], 0, s[16:17]
	global_load_dwordx4 v[100:103], v[70:71], off
	s_lshl_b32 s16, s14, 12
	v_lshl_add_u64 v[72:73], v[66:67], 0, s[16:17]
	global_load_dwordx4 v[144:147], v[72:73], off
	global_load_dwordx4 v[148:151], v[72:73], off offset:1024
	global_load_dwordx4 v[152:155], v[72:73], off offset:2048
	global_load_dwordx4 v[156:159], v[72:73], off offset:3072
	s_add_i32 s14, s4, 2
	s_and_b32 s14, s14, 7
	s_lshl_b32 s16, s14, 5
	v_lshl_add_u64 v[70:71], v[68:69], 0, s[16:17]
	global_load_dwordx4 v[104:107], v[70:71], off
	s_lshl_b32 s16, s14, 12
	v_lshl_add_u64 v[72:73], v[66:67], 0, s[16:17]
	global_load_dwordx4 v[160:163], v[72:73], off
	global_load_dwordx4 v[164:167], v[72:73], off offset:1024
	global_load_dwordx4 v[168:171], v[72:73], off offset:2048
	global_load_dwordx4 v[172:175], v[72:73], off offset:3072
	s_add_i32 s14, s4, 3
	s_and_b32 s14, s14, 7
	s_lshl_b32 s16, s14, 5
	v_lshl_add_u64 v[70:71], v[68:69], 0, s[16:17]
	global_load_dwordx4 v[108:111], v[70:71], off
	s_lshl_b32 s16, s14, 12
	v_lshl_add_u64 v[72:73], v[66:67], 0, s[16:17]
	global_load_dwordx4 v[176:179], v[72:73], off
	global_load_dwordx4 v[180:183], v[72:73], off offset:1024
	global_load_dwordx4 v[184:187], v[72:73], off offset:2048
	global_load_dwordx4 v[188:191], v[72:73], off offset:3072
	s_add_i32 s14, s4, 4
	s_and_b32 s14, s14, 7
	s_lshl_b32 s16, s14, 5
	v_lshl_add_u64 v[70:71], v[68:69], 0, s[16:17]
	global_load_dwordx4 v[112:115], v[70:71], off
	s_lshl_b32 s16, s14, 12
	v_lshl_add_u64 v[72:73], v[66:67], 0, s[16:17]
	global_load_dwordx4 v[192:195], v[72:73], off
	global_load_dwordx4 v[196:199], v[72:73], off offset:1024
	global_load_dwordx4 v[200:203], v[72:73], off offset:2048
	global_load_dwordx4 v[204:207], v[72:73], off offset:3072
	s_add_i32 s14, s4, 5
	s_and_b32 s14, s14, 7
	s_lshl_b32 s16, s14, 5
	v_lshl_add_u64 v[70:71], v[68:69], 0, s[16:17]
	global_load_dwordx4 v[116:119], v[70:71], off
	s_lshl_b32 s16, s14, 12
	v_lshl_add_u64 v[72:73], v[66:67], 0, s[16:17]
	global_load_dwordx4 v[208:211], v[72:73], off
	global_load_dwordx4 v[212:215], v[72:73], off offset:1024
	global_load_dwordx4 v[216:219], v[72:73], off offset:2048
	global_load_dwordx4 v[220:223], v[72:73], off offset:3072
	s_add_i32 s14, s4, 6
	s_and_b32 s14, s14, 7
	s_lshl_b32 s16, s14, 5
	v_lshl_add_u64 v[70:71], v[68:69], 0, s[16:17]
	global_load_dwordx4 v[120:123], v[70:71], off
	s_lshl_b32 s16, s14, 12
	v_lshl_add_u64 v[72:73], v[66:67], 0, s[16:17]
	global_load_dwordx4 v[224:227], v[72:73], off
	global_load_dwordx4 v[228:231], v[72:73], off offset:1024
	global_load_dwordx4 v[232:235], v[72:73], off offset:2048
	global_load_dwordx4 v[236:239], v[72:73], off offset:3072
	s_add_i32 s14, s4, 7
	s_and_b32 s14, s14, 7
	s_lshl_b32 s16, s14, 5
	v_lshl_add_u64 v[70:71], v[68:69], 0, s[16:17]
	global_load_dwordx4 v[124:127], v[70:71], off
	s_lshl_b32 s16, s14, 12
	v_lshl_add_u64 v[72:73], v[66:67], 0, s[16:17]
	global_load_dwordx4 v[240:243], v[72:73], off
	global_load_dwordx4 v[244:247], v[72:73], off offset:1024
	global_load_dwordx4 v[248:251], v[72:73], off offset:2048
	global_load_dwordx4 v[252:255], v[72:73], off offset:3072
	s_lshl_b64 s[0:1], s[0:1], 20
	s_add_u32 s0, s10, s0
	s_addc_u32 s1, s11, s1
	s_lshl_b32 s2, s3, 9
	s_add_u32 s0, s0, s2
	s_addc_u32 s1, s1, 0
	v_lshlrev_b32_e32 v75, 11, v94
	v_lshl_add_u32 v74, v92, 14, 0
	v_lshlrev_b32_e32 v88, 2, v93
	v_add3_u32 v74, v74, v75, v88
	v_add_u32_e32 v77, 0x400, v74
	v_add_u32_e32 v78, 0x1000, v74
	v_add_u32_e32 v79, 0x1400, v74
	v_add_u32_e32 v80, 0x2000, v74
	v_add_u32_e32 v81, 0x2400, v74
	v_add_u32_e32 v82, 0x3000, v74
	v_add_u32_e32 v83, 0x3400, v74
	s_waitcnt vmcnt(35)
	v_mfma_f32_32x32x16_f16 v[4:19], v[96:99], v[128:131], 0
	v_mfma_f32_32x32x16_f16 v[20:35], v[96:99], v[132:135], 0
	v_mfma_f32_32x32x16_f16 v[36:51], v[96:99], v[136:139], 0
	v_mfma_f32_32x32x16_f16 v[52:67], v[96:99], v[140:143], 0
	s_waitcnt vmcnt(30)
	v_mfma_f32_32x32x16_f16 v[4:19], v[100:103], v[144:147], v[4:19]
	v_mfma_f32_32x32x16_f16 v[20:35], v[100:103], v[148:151], v[20:35]
	v_mfma_f32_32x32x16_f16 v[36:51], v[100:103], v[152:155], v[36:51]
	v_mfma_f32_32x32x16_f16 v[52:67], v[100:103], v[156:159], v[52:67]
	s_waitcnt vmcnt(25)
	v_mfma_f32_32x32x16_f16 v[4:19], v[104:107], v[160:163], v[4:19]
	v_mfma_f32_32x32x16_f16 v[20:35], v[104:107], v[164:167], v[20:35]
	v_mfma_f32_32x32x16_f16 v[36:51], v[104:107], v[168:171], v[36:51]
	v_mfma_f32_32x32x16_f16 v[52:67], v[104:107], v[172:175], v[52:67]
	s_waitcnt vmcnt(20)
	v_mfma_f32_32x32x16_f16 v[4:19], v[108:111], v[176:179], v[4:19]
	v_mfma_f32_32x32x16_f16 v[20:35], v[108:111], v[180:183], v[20:35]
	v_mfma_f32_32x32x16_f16 v[36:51], v[108:111], v[184:187], v[36:51]
	v_mfma_f32_32x32x16_f16 v[52:67], v[108:111], v[188:191], v[52:67]
	s_waitcnt vmcnt(15)
	v_mfma_f32_32x32x16_f16 v[4:19], v[112:115], v[192:195], v[4:19]
	v_mfma_f32_32x32x16_f16 v[20:35], v[112:115], v[196:199], v[20:35]
	v_mfma_f32_32x32x16_f16 v[36:51], v[112:115], v[200:203], v[36:51]
	v_mfma_f32_32x32x16_f16 v[52:67], v[112:115], v[204:207], v[52:67]
	s_waitcnt vmcnt(10)
	v_mfma_f32_32x32x16_f16 v[4:19], v[116:119], v[208:211], v[4:19]
	v_mfma_f32_32x32x16_f16 v[20:35], v[116:119], v[212:215], v[20:35]
	v_mfma_f32_32x32x16_f16 v[36:51], v[116:119], v[216:219], v[36:51]
	v_mfma_f32_32x32x16_f16 v[52:67], v[116:119], v[220:223], v[52:67]
	s_waitcnt vmcnt(5)
	v_mfma_f32_32x32x16_f16 v[4:19], v[120:123], v[224:227], v[4:19]
	v_mfma_f32_32x32x16_f16 v[20:35], v[120:123], v[228:231], v[20:35]
	v_mfma_f32_32x32x16_f16 v[36:51], v[120:123], v[232:235], v[36:51]
	v_mfma_f32_32x32x16_f16 v[52:67], v[120:123], v[236:239], v[52:67]
	s_waitcnt vmcnt(0)
	v_mfma_f32_32x32x16_f16 v[4:19], v[124:127], v[240:243], v[4:19]
	v_mfma_f32_32x32x16_f16 v[20:35], v[124:127], v[244:247], v[20:35]
	v_mfma_f32_32x32x16_f16 v[36:51], v[124:127], v[248:251], v[36:51]
	v_mfma_f32_32x32x16_f16 v[52:67], v[124:127], v[252:255], v[52:67]
	s_nop 15
	s_nop 3
	ds_write2_b32 v74, v4, v20 offset0:0 offset1:32
	ds_write2_b32 v74, v36, v52 offset0:64 offset1:96
	ds_write2_b32 v74, v5, v21 offset0:128 offset1:160
	ds_write2_b32 v74, v37, v53 offset0:192 offset1:224
	ds_write2_b32 v77, v6, v22 offset0:0 offset1:32
	ds_write2_b32 v77, v38, v54 offset0:64 offset1:96
	ds_write2_b32 v77, v7, v23 offset0:128 offset1:160
	ds_write2_b32 v77, v39, v55 offset0:192 offset1:224
	ds_write2_b32 v78, v8, v24 offset0:0 offset1:32
	ds_write2_b32 v78, v40, v56 offset0:64 offset1:96
	ds_write2_b32 v78, v9, v25 offset0:128 offset1:160
	ds_write2_b32 v78, v41, v57 offset0:192 offset1:224
	ds_write2_b32 v79, v10, v26 offset0:0 offset1:32
	ds_write2_b32 v79, v42, v58 offset0:64 offset1:96
	ds_write2_b32 v79, v11, v27 offset0:128 offset1:160
	ds_write2_b32 v79, v43, v59 offset0:192 offset1:224
	ds_write2_b32 v80, v12, v28 offset0:0 offset1:32
	ds_write2_b32 v80, v44, v60 offset0:64 offset1:96
	ds_write2_b32 v80, v13, v29 offset0:128 offset1:160
	ds_write2_b32 v80, v45, v61 offset0:192 offset1:224
	ds_write2_b32 v81, v14, v30 offset0:0 offset1:32
	ds_write2_b32 v81, v46, v62 offset0:64 offset1:96
	ds_write2_b32 v81, v15, v31 offset0:128 offset1:160
	ds_write2_b32 v81, v47, v63 offset0:192 offset1:224
	ds_write2_b32 v82, v16, v32 offset0:0 offset1:32
	ds_write2_b32 v82, v48, v64 offset0:64 offset1:96
	ds_write2_b32 v82, v17, v33 offset0:128 offset1:160
	ds_write2_b32 v82, v49, v65 offset0:192 offset1:224
	ds_write2_b32 v83, v18, v34 offset0:0 offset1:32
	ds_write2_b32 v83, v50, v66 offset0:64 offset1:96
	ds_write2_b32 v83, v19, v35 offset0:128 offset1:160
	ds_write2_b32 v83, v51, v67 offset0:192 offset1:224
	v_lshlrev_b32_e32 v64, 4, v0
	v_mov_b32_e32 v65, 0
	v_and_b32_e32 v0, 0x1f0, v64
	s_waitcnt lgkmcnt(0)
	s_barrier
	global_load_dwordx4 v[0:3], v0, s[8:9]
	v_add_u32_e32 v54, 0, v64
	v_add_u32_e32 v4, 0x10000, v54
	v_add_u32_e32 v8, 0x14000, v54
	v_add_u32_e32 v12, 0x18000, v54
	v_add_u32_e32 v16, 0x1c000, v54
	ds_read_b128 v[4:7], v4
	ds_read_b128 v[8:11], v8
	ds_read_b128 v[12:15], v12
	ds_read_b128 v[16:19], v16
	ds_read_b128 v[20:23], v54
	ds_read_b128 v[24:27], v54 offset:8192
	ds_read_b128 v[28:31], v54 offset:16384
	ds_read_b128 v[32:35], v54 offset:24576
	ds_read_b128 v[36:39], v54 offset:32768
	ds_read_b128 v[40:43], v54 offset:40960
	ds_read_b128 v[44:47], v54 offset:49152
	ds_read_b128 v[48:51], v54 offset:57344
	v_lshl_add_u64 v[52:53], s[0:1], 0, v[64:65]
	s_waitcnt vmcnt(0) lgkmcnt(7)
	v_pk_add_f32 v[22:23], v[2:3], v[22:23]
	v_pk_add_f32 v[20:21], v[0:1], v[20:21]
	s_waitcnt lgkmcnt(6)
	v_pk_add_f32 v[2:3], v[2:3], v[26:27]
	v_pk_add_f32 v[0:1], v[0:1], v[24:25]
	s_waitcnt lgkmcnt(5)
	v_pk_add_f32 v[22:23], v[22:23], v[30:31]
	v_pk_add_f32 v[20:21], v[20:21], v[28:29]
	s_waitcnt lgkmcnt(4)
	v_pk_add_f32 v[2:3], v[2:3], v[34:35]
	v_pk_add_f32 v[24:25], v[0:1], v[32:33]
	s_waitcnt lgkmcnt(3)
	v_pk_add_f32 v[0:1], v[22:23], v[38:39]
	v_pk_add_f32 v[20:21], v[20:21], v[36:37]
	s_waitcnt lgkmcnt(2)
	v_pk_add_f32 v[22:23], v[2:3], v[42:43]
	s_waitcnt lgkmcnt(1)
	v_pk_add_f32 v[0:1], v[0:1], v[46:47]
	v_pk_add_f32 v[2:3], v[20:21], v[44:45]
	v_pk_add_f32 v[0:1], v[0:1], v[6:7]
	v_pk_add_f32 v[2:3], v[2:3], v[4:5]
	v_pk_add_f32 v[0:1], v[0:1], v[10:11]
	v_pk_add_f32 v[2:3], v[2:3], v[8:9]
	v_pk_add_f32 v[0:1], v[0:1], v[14:15]
	v_pk_add_f32 v[4:5], v[2:3], v[12:13]
	v_pk_add_f32 v[2:3], v[0:1], v[18:19]
	v_pk_add_f32 v[0:1], v[4:5], v[16:17]
	global_store_dwordx4 v64, v[0:3], s[0:1] sc1
	v_pk_add_f32 v[4:5], v[24:25], v[40:41]
	s_waitcnt lgkmcnt(0)
	v_pk_add_f32 v[8:9], v[22:23], v[50:51]
	v_add_u32_e32 v0, 0x12000, v54
	ds_read_b128 v[0:3], v0
	v_pk_add_f32 v[10:11], v[4:5], v[48:49]
	v_add_u32_e32 v4, 0x16000, v54
	ds_read_b128 v[4:7], v4
	s_waitcnt lgkmcnt(1)
	v_pk_add_f32 v[14:15], v[10:11], v[0:1]
	v_add_u32_e32 v0, 0x1a000, v54
	v_pk_add_f32 v[12:13], v[8:9], v[2:3]
	ds_read_b128 v[0:3], v0
	v_add_u32_e32 v8, 0x1e000, v54
	ds_read_b128 v[8:11], v8
	s_waitcnt lgkmcnt(2)
	v_pk_add_f32 v[6:7], v[12:13], v[6:7]
	v_pk_add_f32 v[4:5], v[14:15], v[4:5]
	s_waitcnt lgkmcnt(1)
	v_pk_add_f32 v[2:3], v[6:7], v[2:3]
	v_pk_add_f32 v[0:1], v[4:5], v[0:1]
	v_add_co_u32_e32 v4, vcc, 0x2000, v52
	s_waitcnt lgkmcnt(0)
	v_pk_add_f32 v[2:3], v[2:3], v[10:11]
	v_pk_add_f32 v[0:1], v[0:1], v[8:9]
	v_addc_co_u32_e32 v5, vcc, 0, v53, vcc
	global_store_dwordx4 v[4:5], v[0:3], off sc1
	s_endpgm
